# combine: slot-id / routing-weight loads issued at the block top with the vector staging loads (one dependent memory round trip less per combine phase)
# baseline (speedup 1.0000x reference)
; __device__ __forceinline__ void combine_ln2_phase(Frame& F, int layer) {
;     ...
;         const int tokb = blk * 64, b = tokb / SEQ;
;         __syncthreads();
;         for (int i = F.tid; i < 1024; i += 512) { PV[i] = modl[(size_t)b * 6144 + 5120 + i] + 1.0f; PV[1024 + i] = lg[i]; PV[2048 + i] = lb[i];
;             if (!lastl) { PV[3072 + i] = modn[(size_t)b * 6144 + 1024 + i] + 1.0f; PV[4096 + i] = modn[(size_t)b * 6144 + i]; } }
;         __syncthreads();
;         const int tw = tokb + wave * 8;
;         int sv; { const int v = tslot[(size_t)tw * 8 + lane]; sv = ts[v >> 14] * 256 + (v & (CAP - 1)); }
;         const float wvv = ((const float*)(F.ws + WS_WL))[(size_t)tw * 8 + lane] * (1.0f / 32.0f);
.LBB0_1784:
	s_barrier
	s_lshl_b32 s0, s10, 6
	s_add_i32 s50, s0, s7
	s_ashr_i32 s51, s50, 31
	s_lshl_b64 s[0:1], s[50:51], 5
	v_lshl_or_b32 v4, v28, 2, s0
	v_mov_b32_e32 v5, s1
	v_lshl_add_u64 v[6:7], s[30:31], 0, v[4:5]
	global_load_dword v206, v[6:7], off
	v_lshl_add_u64 v[4:5], s[74:75], 0, v[4:5]
	global_load_dword v207, v[4:5], off
	s_and_saveexec_b64 s[0:1], s[40:41]
	s_cbranch_execz .LBB0_1789
	s_ashr_i32 s11, s10, 31
	s_lshr_b32 s11, s11, 27
	s_add_i32 s11, s10, s11
	s_ashr_i32 s11, s11, 5
	s_mul_hi_i32 s22, s11, 0x6000
	s_mulk_i32 s11, 0x6000
	v_readlane_b32 s25, v254, 28
	s_add_u32 s50, s25, s11
	v_readlane_b32 s25, v254, 29
	s_addc_u32 s51, s25, s22
	v_readlane_b32 s25, v254, 30
	s_add_u32 s52, s25, s11
	v_readlane_b32 s25, v254, 31
	s_addc_u32 s53, s25, s22
	v_readlane_b32 s25, v254, 32
	s_add_u32 s54, s25, s11
	v_readlane_b32 s11, v254, 33
	s_addc_u32 s55, s11, s22
	s_mov_b64 s[56:57], 0
	s_mov_b64 s[60:61], s[48:49]
	s_mov_b64 s[62:63], s[46:47]
	s_waitcnt vmcnt(2)
	v_lshl_add_u64 v[6:7], s[50:51], 0, v[36:37]
	global_load_dword v8, v[6:7], off
	global_load_dword v9, v[6:7], off offset:2048
	v_lshl_add_u64 v[6:7], s[60:61], 0, v[36:37]
	global_load_dword v10, v[6:7], off
	global_load_dword v11, v[6:7], off offset:2048
	v_lshl_add_u64 v[6:7], s[62:63], 0, v[36:37]
	global_load_dword v12, v[6:7], off
	global_load_dword v13, v[6:7], off offset:2048
	v_add_u32_e32 v4, 0x800, v82
	s_and_b64 vcc, exec, s[44:45]
	s_cbranch_vccz .Lcpv_last
	v_lshl_add_u64 v[6:7], s[52:53], 0, v[36:37]
	global_load_dword v14, v[6:7], off
	global_load_dword v15, v[6:7], off offset:2048
	v_lshl_add_u64 v[6:7], s[54:55], 0, v[36:37]
	global_load_dword v16, v[6:7], off
	global_load_dword v17, v[6:7], off offset:2048
	s_waitcnt vmcnt(0)
	v_add_f32_e32 v14, 1.0, v14
	v_add_f32_e32 v15, 1.0, v15
	ds_write2st64_b32 v82, v14, v16 offset0:48 offset1:64
	ds_write2st64_b32 v4, v15, v17 offset0:48 offset1:64

; __device__ __forceinline__ void combine_ln2_phase(Frame& F, int layer) {
;     ...
;         const int tw = tokb + wave * 8;
;         int sv; { const int v = tslot[(size_t)tw * 8 + lane]; sv = ts[v >> 14] * 256 + (v & (CAP - 1)); }
;         const float wvv = ((const float*)(F.ws + WS_WL))[(size_t)tw * 8 + lane] * (1.0f / 32.0f);
;         pg8::u32x2_t ys[18]; u32x4 xs[2];
.LBB0_1789:
	s_or_b64 exec, exec, s[0:1]
	s_lshl_b32 s0, s10, 6
	s_add_i32 s50, s0, s7
	s_ashr_i32 s51, s50, 31
	s_lshl_b64 s[0:1], s[50:51], 5
	s_waitcnt vmcnt(1)
	v_lshl_or_b32 v4, v28, 2, s0
	v_mov_b32_e32 v5, s1
	v_lshl_add_u64 v[6:7], s[30:31], 0, v[4:5]
	s_waitcnt lgkmcnt(0)
	s_barrier
	s_add_i32 s0, s50, s8
	s_ashr_i32 s1, s0, 31
	s_lshl_b64 s[0:1], s[0:1], 10
	s_mov_b32 s11, 1
	s_mov_b32 s25, 7
	s_waitcnt vmcnt(1)
	v_ashrrev_i32_e32 v7, 14, v206
	v_lshl_add_u32 v7, v7, 2, 0
	v_add_u32_e32 v7, 0x21080, v7
	ds_read_b32 v7, v7
	v_and_b32_e32 v6, 0x3fff, v206
	s_waitcnt vmcnt(0)
	v_mul_f32_e32 v84, 0x3d000000, v207
	s_waitcnt lgkmcnt(0)
	v_lshl_add_u32 v83, v7, 8, v6
	s_nop 0
	v_readlane_b32 s28, v83, 0
	s_ashr_i32 s29, s28, 31
	s_lshl_b64 s[28:29], s[28:29], 10
	v_lshl_add_u64 v[4:5], v[30:31], 0, s[28:29]
	v_readlane_b32 s28, v83, 1
	s_ashr_i32 s29, s28, 31
	s_lshl_b64 s[28:29], s[28:29], 10
	global_load_dwordx2 v[50:51], v[4:5], off nt
	global_load_dwordx2 v[44:45], v[4:5], off offset:512 nt
	v_lshl_add_u64 v[4:5], v[30:31], 0, s[28:29]
	v_readlane_b32 s28, v83, 2
	s_ashr_i32 s29, s28, 31
	s_lshl_b64 s[28:29], s[28:29], 10
	global_load_dwordx2 v[42:43], v[4:5], off nt
	global_load_dwordx2 v[38:39], v[4:5], off offset:512 nt
	v_lshl_add_u64 v[4:5], v[30:31], 0, s[28:29]
	v_readlane_b32 s28, v83, 3
	s_ashr_i32 s29, s28, 31
	s_lshl_b64 s[28:29], s[28:29], 10
	global_load_dwordx2 v[60:61], v[4:5], off nt
	global_load_dwordx2 v[52:53], v[4:5], off offset:512 nt
	v_lshl_add_u64 v[4:5], v[30:31], 0, s[28:29]
	v_readlane_b32 s28, v83, 4
	s_ashr_i32 s29, s28, 31
	s_lshl_b64 s[28:29], s[28:29], 10
	global_load_dwordx2 v[48:49], v[4:5], off nt
	global_load_dwordx2 v[40:41], v[4:5], off offset:512 nt
	v_lshl_add_u64 v[4:5], v[30:31], 0, s[28:29]
	v_readlane_b32 s28, v83, 5
	s_ashr_i32 s29, s28, 31
	s_lshl_b64 s[28:29], s[28:29], 10
	global_load_dwordx2 v[64:65], v[4:5], off nt
	global_load_dwordx2 v[58:59], v[4:5], off offset:512 nt
	v_lshl_add_u64 v[4:5], v[30:31], 0, s[28:29]
	v_readlane_b32 s28, v83, 6
	s_ashr_i32 s29, s28, 31
	s_lshl_b64 s[28:29], s[28:29], 10
	global_load_dwordx2 v[56:57], v[4:5], off nt
	global_load_dwordx2 v[46:47], v[4:5], off offset:512 nt
	v_lshl_add_u64 v[4:5], v[30:31], 0, s[28:29]
	v_readlane_b32 s28, v83, 7
	s_ashr_i32 s29, s28, 31
	s_lshl_b64 s[28:29], s[28:29], 10
	global_load_dwordx2 v[68:69], v[4:5], off nt
	global_load_dwordx2 v[62:63], v[4:5], off offset:512 nt
	v_lshl_add_u64 v[4:5], v[30:31], 0, s[28:29]
	global_load_dwordx2 v[54:55], v[4:5], off nt
	global_load_dwordx2 v[66:67], v[4:5], off offset:512 nt
	v_lshl_add_u64 v[4:5], v[30:31], 0, s[0:1]
	s_lshl_b64 s[0:1], s[50:51], 11
	v_lshl_add_u64 v[8:9], v[32:33], 0, s[0:1]
	global_load_dwordx2 v[72:73], v[4:5], off nt
	global_load_dwordx2 v[70:71], v[4:5], off offset:512 nt
	s_nop 0
	global_load_dwordx4 v[4:7], v[8:9], off nt
	s_nop 0
	global_load_dwordx4 v[8:11], v[8:9], off offset:1024 nt
	s_branch .LBB0_1791
